# mixer A K/V tile loops: LDS-DMA (global_load_lds_dwordx4) into two 8 KiB stages per wave, two tiles in flight, counted vmcnt(8), source-side K swizzle
# speedup vs baseline: 1.0133x; 1.0116x over previous
; #define LAS __attribute__((address_space(3)))
; __device__ __forceinline__ void band_branch_fast(f32x16& o0, f32x16& o1, f32x4& lsum, unsigned& orw, const bf16x8 (&qf)[4], ...
;     const unsigned one2 = ((lane & 15) == ((lane >> 4) & 1)) ? 0x3F803F80u : 0u;
;     const bf16x8 onesA = __builtin_bit_cast(bf16x8, (v4u){one2, one2, one2, one2});
;     int kt_lo = 0, kt_hi = ntiles;
;     if (kb_first < 0) kt_lo = (-kb_first) >> 5;
;     { const int mx = (L - kb_first) >> 5; if (mx < kt_hi) kt_hi = mx; }
;     const int i5 = lane & 31, hh = lane >> 5;
;     const int pi = (i5 & 0x13) | (((i5 >> 2) & 1) << 3) | (((i5 >> 3) & 1) << 2);
;     const int vr = lane >> 3, vc = lane & 7;
;     LAS unsigned char* kst = vst + 4096;
;     const LAS unsigned char* trb = vst + (8 * hh + ((lane & 15) >> 2)) * 128 + (16 * ((lane >> 4) & 1) + 4 * (lane & 3)) * 2;
;     const LAS unsigned char* krd = kst + pi * 128;
; __device__ __forceinline__ void mixer_a_phase(const bf16* AQ, const bf16* AK, const bf16* AV  , bf16* O, float* ST, float* ML, const float* rel_bias, LAS unsigned char* lds, int G, int blk, int tid, int lane, int wave) {
;     LAS float* tab = (LAS float*)lds; LAS unsigned char* vst = lds + BAND_VST_OFF + wave * 8192;
;     constexpr float M_FAST = 127.0f;
;     int cur_h = -1;
;     for (int u = blk; u < 512; u += G) {
;         const int h = u & 7, v = u >> 3, b = v >> 4, a = v & 15;
;         if (h != cur_h) {
;             __syncthreads();
;             for (int idx = tid; idx < 3 * TA_LEN; idx += NWAVES * 64) { const int br = idx / TA_LEN, i = idx % TA_LEN - TA_OFF, dil = br == 0 ? 1 : (br == 1 ? 4 : 16);
;                 tab[idx] = (i >= 0 && i <= 128) ? (rel_bias[h * 32 + t5_bucket((i - 64) * dil)] * LOG2E + 64.0f) * KAPPA : -1.0f; }
;             __syncthreads(); cur_h = h;
;         }
;         const int i5 = lane & 31, hh = lane >> 5;
;         const size_t tb0 = (size_t)b * SEQ;
;         const bf16* Kb = AK + tb0 * 512 + h * 64; const bf16* Vb = AV + tb0 * 512 + h * 64;
;         bf16x8 qn[4];
;         { const bf16* qp = AQ + (tb0 + 512 * a + 32 * wave + i5) * 512 + h * 64 + 8 * hh;
.LBB0_343:
	v_readlane_b32 s0, v254, 10
	v_readlane_b32 s4, v255, 17
	s_cmpk_gt_i32 s0, 0x1ff
	v_readlane_b32 s5, v255, 18
	s_cbranch_scc1 .LBB0_423
	v_readlane_b32 s0, v254, 0
	v_readlane_b32 s1, v254, 1
	s_add_u32 s12, s0, 0x29400000
	v_readlane_b32 s8, v254, 59
	s_addc_u32 s13, s1, 0
	s_lshl_b32 s0, s8, 14
	v_bfe_u32 v6, v1, 5, 1
	v_lshlrev_b32_e32 v8, 5, v1
	s_add_i32 s0, s0, 0
	v_lshlrev_b32_e32 v7, 10, v6
	v_and_b32_e32 v8, 0x180, v8
	v_add3_u32 v192, s0, v7, v8
	v_and_b32_e32 v8, 19, v1
	v_lshrrev_b32_e32 v9, 1, v1
	v_bfe_u32 v5, v1, 4, 1
	v_and_or_b32 v8, v9, 4, v8
	v_bfe_u32 v196, v1, 3, 3
	v_and_b32_e32 v9, 15, v1
	v_lshl_add_u32 v194, v5, 5, v192
	v_cmp_eq_u32_e32 vcc, v9, v5
	v_bitop3_b32 v5, v196, v1, 7 bitop3:0x78
	v_lshl_add_u32 v198, v5, 4, s0
	v_bitop3_b32 v5, v8, v6, 7 bitop3:0x6c
	v_lshlrev_b32_e32 v200, 4, v5
	v_or_b32_e32 v5, 2, v6
	v_bitop3_b32 v5, v8, v5, 7 bitop3:0x6c
	v_lshlrev_b32_e32 v201, 4, v5
	v_or_b32_e32 v5, 4, v6
	v_bitop3_b32 v5, v8, v5, 7 bitop3:0x6c
	v_lshlrev_b32_e32 v7, 3, v1
	v_lshlrev_b32_e32 v202, 4, v5
	v_or_b32_e32 v5, 6, v6
	v_and_b32_e32 v193, 24, v7
	v_lshlrev_b32_e32 v7, 1, v1
	v_bitop3_b32 v5, v8, v5, 7 bitop3:0x6c
	v_and_b32_e32 v2, 63, v1
	v_and_or_b32 v7, v7, 8, v8
	v_lshlrev_b32_e32 v203, 4, v5
	v_and_b32_e32 v5, 16, v1
	v_lshlrev_b32_e32 v8, 2, v1
	v_cmp_gt_u32_e64 s[6:7], 32, v2
	v_and_or_b32 v2, v8, 12, v5
	s_movk_i32 s1, 0xf00
	v_mov_b32_e32 v3, 0
	v_lshl_add_u32 v195, v7, 7, s0
	v_and_b32_e32 v7, 7, v1
	v_lshlrev_b32_e32 v204, 1, v2
	v_and_b32_e32 v2, 32, v1
	v_cmp_gt_i32_e64 s[2:3], s1, v1
	v_and_b32_e32 v141, 31, v1
	s_lshl_b32 s1, s8, 5
	v_readlane_b32 s9, v254, 6
	v_lshlrev_b32_e32 v142, 3, v7
	v_lshlrev_b32_e32 v144, 4, v7
	v_lshlrev_b32_e32 v6, 1, v2
	v_mov_b32_e32 v7, v3
	v_readlane_b32 s10, v255, 21
	s_cmpk_lt_u32 s9, 0x400
	v_cmp_eq_u32_e64 s[4:5], 0, v5
	v_lshl_add_u64 v[146:147], s[92:93], 0, v[6:7]
	v_mul_i32_i24_e32 v5, -4, v141
	v_readlane_b32 s11, v255, 22
	v_lshlrev_b32_e32 v6, 2, v141
	s_cselect_b64 s[18:19], -1, 0
	v_add_u32_e32 v199, s0, v144
	v_lshl_add_u64 v[148:149], s[10:11], 0, v[2:3]
	v_sub_u32_e32 v6, v2, v6
	v_lshl_add_u32 v2, v5, 2, v2
	s_and_b32 s0, s8, 0x3fffffc
	v_subrev_u32_e32 v2, s0, v2
	s_bfe_u32 s38, s9, 0x20006
	v_add_u32_e32 v2, 0, v2
	v_add_u32_e32 v210, 0x1c00, v2
	v_lshl_or_b32 v2, v196, 2, s38
	v_or_b32_e32 v211, 0xffffffe0, v2
	v_or_b32_e32 v212, 0xffffffc0, v2
	v_or_b32_e32 v213, 0xffffffa0, v2
	v_or_b32_e32 v214, 0xffffff80, v2
	v_mbcnt_lo_u32_b32 v2, -1, 0
	v_lshrrev_b32_e32 v4, 2, v1
	v_mov_b32_e32 v10, 0x3f803f80
	v_add_u32_e32 v6, 0, v6
	v_mbcnt_hi_u32_b32 v2, -1, v2
	v_and_b32_e32 v4, 8, v4
	v_lshlrev_b32_e32 v143, 4, v141
	v_cndmask_b32_e32 v70, 0, v10, vcc
	v_add_u32_e32 v206, 0x800, v6
	v_or_b32_e32 v7, s1, v196
	v_add_u32_e32 v208, 0x3000, v6
	v_lshl_add_u32 v6, v196, 4, s8
	v_and_or_b32 v2, v2, 64, v9
	v_readlane_b32 s43, v254, 10
	s_mov_b32 s17, 0
	v_or_b32_e32 v138, s1, v141
	v_mov_b32_e32 v139, v3
	v_add_u32_e32 v140, s8, v143
	v_mov_b32_e32 v71, v70
	v_mov_b32_e32 v72, v70
	v_mov_b32_e32 v73, v70
	v_lshlrev_b32_e32 v197, 7, v196
	v_add_u32_e32 v205, 0, v8
	v_subrev_u32_e32 v207, 32, v7
	v_add_u32_e32 v209, 0xfffffe00, v6
	v_mov_b32_e32 v145, v3
	s_mov_b32 s45, -1
	v_mov_b32_e32 v215, 0x42800000
	v_lshlrev_b32_e32 v150, 1, v4
	s_mov_b32 s39, 0xda24260
	s_mov_b64 s[20:21], 0x20000
	s_mov_b32 s40, 0x42000000
	s_mov_b32 s41, 0xc3e00000
	v_lshlrev_b32_e32 v216, 2, v2
	v_mov_b32_e32 v217, 0x43e00000
	s_mov_b32 s42, s43
	s_branch .LBB0_346

; #define LAS __attribute__((address_space(3)))
; #define BA_LOAD(kn, vn, kt_) do { const int kb_ = kb_first + 32 * (kt_); \
;         _Pragma("unroll") for (int ii = 0; ii < 4; ++ii) { const size_t row_ = (size_t)(res + dil * (kb_ + vr + 8 * ii)); \
;             kn[ii] = *(const v4u*)(Kb + row_ * kpitch + 8 * vc); vn[ii] = *(const v4u*)(Vb + row_ * vpitch + 8 * vc); } } while (0)
; __device__ __forceinline__ void band_branch_fast(f32x16& o0, f32x16& o1, f32x4& lsum, unsigned& orw, const bf16x8 (&qf)[4], ...
;     ...
;     int kt_lo = 0, kt_hi = ntiles;
;     if (kb_first < 0) kt_lo = (-kb_first) >> 5;
;     { const int mx = (L - kb_first) >> 5; if (mx < kt_hi) kt_hi = mx; }
;     const int i5 = lane & 31, hh = lane >> 5;
;     const int pi = (i5 & 0x13) | (((i5 >> 2) & 1) << 3) | (((i5 >> 3) & 1) << 2);
;     const int vr = lane >> 3, vc = lane & 7;
;     LAS unsigned char* kst = vst + 4096;
;     const LAS unsigned char* trb = vst + (8 * hh + ((lane & 15) >> 2)) * 128 + (16 * ((lane >> 4) & 1) + 4 * (lane & 3)) * 2;
;     const LAS unsigned char* krd = kst + pi * 128;
;     v4u kn[4], vn[4];
;     ...
;     if (kt_lo < kt_hi) BA_LOAD(kn, vn, kt_lo);
; __device__ __forceinline__ void mixer_a_phase(const bf16* AQ, const bf16* AK, const bf16* AV  , bf16* O, float* ST, float* ML, const float* rel_bias, LAS unsigned char* lds, int G, int blk, int tid, int lane, int wave) {
;     ...
;             const int q0 = 512 * a + 32 * tile, tq = q0 + i5;
;             bf16x8 qf[4];
; #pragma unroll
;             for (int d0 = 0; d0 < 4; ++d0) qf[d0] = qn[d0];
;             { const bool more = tile + NWAVES < 16; const bf16* qp = more ? AQ + (tb0 + tq + 32 * NWAVES) * 512 + h * 64 + 8 * hh : AQ + (tb0 + 512 * a + 16 * i5 + wave) * 512 + h * 64 + 8 * hh;
; #pragma unroll
;               for (int d0 = 0; d0 < 4; ++d0) qn[d0] = *(const bf16x8*)(qp + 16 * d0); }
;             f32x16 o0 = {}, o1 = {}; f32x4 lsum = {0.f, 0.f, 0.f, 0.f}; unsigned orw = 0u; float m = M_FAST, l;
;             band_branch_fast(o0, o1, lsum, orw, qf, Kb, 512, Vb, 512, 1, 0, SEQ, q0 - 64, 5, tab, -tq + 64 + TA_OFF + 8 * hh, vst, lane);
.LBB0_359:
	s_lshl_b32 s15, s14, 5
	s_add_i32 s33, s15, s0
	v_or_b32_e32 v2, s33, v141
	v_lshl_add_u64 v[158:159], s[22:23], 0, v[2:3]
	v_readlane_b32 s34, v255, 7
	s_cmp_gt_u32 s14, 7
	v_lshlrev_b64 v[4:5], 10, v[158:159]
	v_readlane_b32 s35, v255, 8
	s_cselect_b64 s[26:27], -1, 0
	s_cmp_lt_u32 s14, 8
	v_lshl_add_u64 v[4:5], s[34:35], 0, v[4:5]
	s_mov_b64 s[34:35], 0x40000
	v_lshl_add_u64 v[4:5], v[4:5], 0, s[34:35]
	s_cselect_b64 vcc, -1, 0
	v_cndmask_b32_e32 v5, v153, v5, vcc
	v_cndmask_b32_e32 v4, v152, v4, vcc
	s_lshl_b32 s16, s24, 1
	v_lshl_add_u64 v[4:5], v[4:5], 0, s[16:17]
	v_mov_b32_e32 v151, v3
	v_lshl_add_u64 v[4:5], v[4:5], 0, v[150:151]
	global_load_dwordx4 v[74:77], v[4:5], off
	global_load_dwordx4 v[78:81], v[4:5], off offset:32
	global_load_dwordx4 v[82:85], v[4:5], off offset:64
	global_load_dwordx4 v[86:89], v[4:5], off offset:96
	s_sub_i32 s15, 64, s33
	v_sub_co_u32_e64 v2, s[34:35], s33, 64
	s_lshr_b32 s15, s15, 5
	s_and_b64 s[34:35], s[34:35], exec
	s_cselect_b32 s15, s15, 0
	s_sub_i32 s16, 0x2040, s33
	s_ashr_i32 s16, s16, 5
	s_min_i32 s16, s16, 5
	s_cmp_lt_i32 s15, s16
	s_cselect_b64 s[34:35], -1, 0
	s_cmp_ge_i32 s15, s16
	s_cbranch_scc1 .LBB0_364
	s_lshl_b32 s33, s15, 5
	v_add_u32_e32 v4, s33, v2
	v_or_b32_e32 v4, v4, v196
	v_and_b32_e32 v110, 7, v1
	v_xor_b32_e32 v111, v110, v196
	v_sub_u32_e32 v110, v111, v110
	v_lshlrev_b32_e32 v112, 4, v110
	v_ashrrev_i32_e32 v113, 31, v112
	v_lshl_add_u64 v[114:115], v[154:155], 0, v[112:113]
	v_readlane_b32 s98, v254, 59
	s_mov_b64 s[100:101], 0x8000
	v_mov_b32_e32 v110, v4
	v_ashrrev_i32_e32 v111, 31, v110
	v_lshlrev_b64 v[110:111], 10, v[110:111]
	v_lshl_add_u64 v[94:95], v[114:115], 0, v[110:111]
	v_lshl_add_u64 v[96:97], v[156:157], 0, v[110:111]
	v_or_b32_e32 v110, 8, v4
	v_ashrrev_i32_e32 v111, 31, v110
	v_lshlrev_b64 v[110:111], 10, v[110:111]
	v_lshl_add_u64 v[98:99], v[114:115], 0, v[110:111]
	v_lshl_add_u64 v[100:101], v[156:157], 0, v[110:111]
	v_or_b32_e32 v110, 16, v4
	v_ashrrev_i32_e32 v111, 31, v110
	v_lshlrev_b64 v[110:111], 10, v[110:111]
	v_lshl_add_u64 v[102:103], v[114:115], 0, v[110:111]
	v_lshl_add_u64 v[104:105], v[156:157], 0, v[110:111]
	v_or_b32_e32 v110, 24, v4
	v_ashrrev_i32_e32 v111, 31, v110
	v_lshlrev_b64 v[110:111], 10, v[110:111]
	v_lshl_add_u64 v[106:107], v[114:115], 0, v[110:111]
	v_lshl_add_u64 v[108:109], v[156:157], 0, v[110:111]
	s_lshl_b32 s98, s98, 14
	s_add_i32 s98, s98, 0x4000
	s_mov_b32 s99, 0
	s_add_i32 m0, s98, 0x1000
	s_nop 0
	global_load_lds_dwordx4 v[94:95], off
	s_add_i32 m0, s98, 0x0
	v_lshl_add_u64 v[94:95], v[94:95], 0, s[100:101]
	global_load_lds_dwordx4 v[96:97], off
	s_add_i32 m0, s98, 0x1400
	v_lshl_add_u64 v[96:97], v[96:97], 0, s[100:101]
	global_load_lds_dwordx4 v[98:99], off
	s_add_i32 m0, s98, 0x400
	v_lshl_add_u64 v[98:99], v[98:99], 0, s[100:101]
	global_load_lds_dwordx4 v[100:101], off
	s_add_i32 m0, s98, 0x1800
	v_lshl_add_u64 v[100:101], v[100:101], 0, s[100:101]
	global_load_lds_dwordx4 v[102:103], off
	s_add_i32 m0, s98, 0x800
	v_lshl_add_u64 v[102:103], v[102:103], 0, s[100:101]
	global_load_lds_dwordx4 v[104:105], off
	s_add_i32 m0, s98, 0x1c00
	v_lshl_add_u64 v[104:105], v[104:105], 0, s[100:101]
	global_load_lds_dwordx4 v[106:107], off
	s_add_i32 m0, s98, 0xc00
	v_lshl_add_u64 v[106:107], v[106:107], 0, s[100:101]
	global_load_lds_dwordx4 v[108:109], off
	v_lshl_add_u64 v[108:109], v[108:109], 0, s[100:101]
	s_add_i32 s46, s15, 1
	s_cmp_lt_i32 s46, s16
	s_cbranch_scc0 .Lmx1_p1
	s_add_i32 m0, s98, 0x3000
	s_nop 0
	global_load_lds_dwordx4 v[94:95], off
	s_add_i32 m0, s98, 0x2000
	v_lshl_add_u64 v[94:95], v[94:95], 0, s[100:101]
	global_load_lds_dwordx4 v[96:97], off
	s_add_i32 m0, s98, 0x3400
	v_lshl_add_u64 v[96:97], v[96:97], 0, s[100:101]
	global_load_lds_dwordx4 v[98:99], off
	s_add_i32 m0, s98, 0x2400
	v_lshl_add_u64 v[98:99], v[98:99], 0, s[100:101]
	global_load_lds_dwordx4 v[100:101], off
	s_add_i32 m0, s98, 0x3800
	v_lshl_add_u64 v[100:101], v[100:101], 0, s[100:101]
	global_load_lds_dwordx4 v[102:103], off
	s_add_i32 m0, s98, 0x2800
	v_lshl_add_u64 v[102:103], v[102:103], 0, s[100:101]
	global_load_lds_dwordx4 v[104:105], off
	s_add_i32 m0, s98, 0x3c00
	v_lshl_add_u64 v[104:105], v[104:105], 0, s[100:101]
	global_load_lds_dwordx4 v[106:107], off
	s_add_i32 m0, s98, 0x2c00
	v_lshl_add_u64 v[106:107], v[106:107], 0, s[100:101]
	global_load_lds_dwordx4 v[108:109], off
	v_lshl_add_u64 v[108:109], v[108:109], 0, s[100:101]
; #define LAS __attribute__((address_space(3)))
; #define BA_TR(off_) __builtin_bit_cast(s16x4, __builtin_amdgcn_ds_read_tr16_b64_v4i16((LAS v4i16_t*)(trb + (off_))))
; #define BA_TR(off_) __builtin_bit_cast(s16x4, __builtin_amdgcn_ds_read_tr16_b64_v4i16((LAS v4i16_t*)(trb + (off_))))
; __device__ __forceinline__ void band_branch_fast(f32x16& o0, f32x16& o1, f32x4& lsum, unsigned& orw, const bf16x8 (&qf)[4], ...
;     ...
;     for (int kt = kt_lo; kt < kt_hi; ++kt) {
; #pragma unroll
;         for (int ii = 0; ii < 4; ++ii) { const int r_ = vr + 8 * ii; *(LAS v4u*)(kst + r_ * 128 + ((vc ^ (r_ & 7)) * 16)) = kn[ii]; *(LAS v4u*)(vst + r_ * 128 + vc * 16) = vn[ii]; }
;         if (kt + 1 < kt_hi) BA_LOAD(kn, vn, kt + 1);
;         bf16x8 kf[4];
; #pragma unroll
;         for (int d0 = 0; d0 < 4; ++d0) kf[d0] = *(const LAS bf16x8*)(krd + (((2 * d0 + hh) ^ (pi & 7)) * 16));
;         const LAS float* tp = tab + (kb_first + 32 * kt + tboff);
;         f32x16 s;
; #pragma unroll
;         for (int r = 0; r < 16; ++r) s[r] = tp[(r & 7) + 16 * (r >> 3)];
;         s16x4 vt[8];
; #pragma unroll
;         for (int i = 0; i < 8; ++i) vt[i] = BA_TR((i >> 2) * 2048 + ((i >> 1) & 1) * 64 + (i & 1) * 512);
;         __builtin_amdgcn_sched_barrier(0);
; #pragma unroll
;         for (int d0 = 0; d0 < 4; ++d0) s = __builtin_amdgcn_mfma_f32_32x32x16_bf16(kf[d0], qf[d0], s, 0, 0, 0);
;         __builtin_amdgcn_sched_barrier(0);
;         v4u p0, p1;
;     ...
;         p0.x = BA_PKN(s[0], s[1]); p0.y = BA_PKN(s[2], s[3]); p0.z = BA_PKN(s[4], s[5]); p0.w = BA_PKN(s[6], s[7]);
;         p1.x = BA_PKN(s[8], s[9]); p1.y = BA_PKN(s[10], s[11]); p1.z = BA_PKN(s[12], s[13]); p1.w = BA_PKN(s[14], s[15]);
;     ...
;         orw |= (p0.x | p0.y | p0.z) | (p0.w | p1.x | p1.y) | (p1.z | p1.w);
;         const bf16x8 pk0 = __builtin_bit_cast(bf16x8, p0), pk1 = __builtin_bit_cast(bf16x8, p1);
;         lsum = __builtin_amdgcn_mfma_f32_16x16x32_bf16(onesA, pk0, lsum, 0, 0, 0); lsum = __builtin_amdgcn_mfma_f32_16x16x32_bf16(onesA, pk1, lsum, 0, 0, 0);
;         o0 = __builtin_amdgcn_mfma_f32_32x32x16_bf16(BA_VF(0), pk0, o0, 0, 0, 0); o1 = __builtin_amdgcn_mfma_f32_32x32x16_bf16(BA_VF(2), pk0, o1, 0, 0, 0);
;         o0 = __builtin_amdgcn_mfma_f32_32x32x16_bf16(BA_VF(4), pk1, o0, 0, 0, 0); o1 = __builtin_amdgcn_mfma_f32_32x32x16_bf16(BA_VF(6), pk1, o1, 0, 0, 0);
.Lmx1_p1:
	v_mov_b32_e32 v20, 0
	v_lshl_add_u32 v69, s15, 7, v206
	v_mov_b32_e32 v127, 0
	v_mov_b32_e32 v126, v162
	s_mov_b32 s46, s15
	v_mov_b32_e32 v21, v20
	v_mov_b32_e32 v22, v20
	v_mov_b32_e32 v23, v20
	v_mov_b32_e32 v24, v20
	v_mov_b32_e32 v25, v20
	v_mov_b32_e32 v26, v20
	v_mov_b32_e32 v27, v20
	v_mov_b32_e32 v28, v20
	v_mov_b32_e32 v29, v20
	v_mov_b32_e32 v30, v20
	v_mov_b32_e32 v31, v20
	v_mov_b32_e32 v32, v20
	v_mov_b32_e32 v33, v20
	v_mov_b32_e32 v34, v20
	v_mov_b32_e32 v35, v20
	v_mov_b32_e32 v4, v20
	v_mov_b32_e32 v5, v20
	v_mov_b32_e32 v6, v20
	v_mov_b32_e32 v7, v20
	v_mov_b32_e32 v8, v20
	v_mov_b32_e32 v9, v20
	v_mov_b32_e32 v10, v20
	v_mov_b32_e32 v11, v20
	v_mov_b32_e32 v12, v20
	v_mov_b32_e32 v13, v20
	v_mov_b32_e32 v14, v20
	v_mov_b32_e32 v15, v20
	v_mov_b32_e32 v16, v20
	v_mov_b32_e32 v17, v20
	v_mov_b32_e32 v18, v20
	v_mov_b32_e32 v19, v20
	v_mov_b32_e32 v90, v20
	v_mov_b32_e32 v91, v20
	v_mov_b32_e32 v92, v20
	v_mov_b32_e32 v93, v20
	s_branch .LBB0_362
.LBB0_361:
	v_add3_u32 v36, v195, v200, s99
	v_add3_u32 v37, v195, v201, s99
	ds_read_b128 v[128:131], v36 offset:20480
	ds_read_b128 v[132:135], v37 offset:20480
	v_add3_u32 v36, v195, v202, s99
	v_add3_u32 v37, v195, v203, s99
	ds_read_b128 v[164:167], v36 offset:20480
	ds_read_b128 v[168:171], v37 offset:20480
	ds_read2_b32 v[36:37], v69 offset1:1
	ds_read2_b32 v[38:39], v69 offset0:2 offset1:3
	ds_read2_b32 v[40:41], v69 offset0:4 offset1:5
	ds_read2_b32 v[42:43], v69 offset0:6 offset1:7
	ds_read2_b32 v[44:45], v69 offset0:16 offset1:17
	ds_read2_b32 v[46:47], v69 offset0:18 offset1:19
	ds_read2_b32 v[48:49], v69 offset0:20 offset1:21
	ds_read2_b32 v[50:51], v69 offset0:22 offset1:23
	v_add3_u32 v136, v194, v193, s99
	ds_read_b64_tr_b16 v[172:173], v136 offset:16384
	ds_read_b64_tr_b16 v[174:175], v136 offset:16896
	ds_read_b64_tr_b16 v[178:179], v136 offset:16960
	ds_read_b64_tr_b16 v[176:177], v136 offset:16448
	ds_read_b64_tr_b16 v[180:181], v136 offset:18432
	ds_read_b64_tr_b16 v[182:183], v136 offset:18944
	ds_read_b64_tr_b16 v[186:187], v136 offset:19008
	ds_read_b64_tr_b16 v[184:185], v136 offset:18496
	s_waitcnt lgkmcnt(8)
	v_mfma_f32_32x32x16_bf16 v[36:51], v[128:131], v[52:55], v[36:51]
	v_mfma_f32_32x32x16_bf16 v[36:51], v[132:135], v[56:59], v[36:51]
	v_mfma_f32_32x32x16_bf16 v[36:51], v[164:167], v[60:63], v[36:51]
	v_mfma_f32_32x32x16_bf16 v[36:51], v[168:171], v[64:67], v[36:51]
	s_waitcnt lgkmcnt(0)
	s_add_i32 s46, s46, 1
	s_cmp_lt_i32 s46, s16
	s_cbranch_scc0 .Lmx1_skip
	s_add_i32 m0, s98, 0x1000
	s_nop 0
	global_load_lds_dwordx4 v[94:95], off
	s_add_i32 m0, s98, 0x0
	v_lshl_add_u64 v[94:95], v[94:95], 0, s[100:101]
	global_load_lds_dwordx4 v[96:97], off
	s_add_i32 m0, s98, 0x1400
	v_lshl_add_u64 v[96:97], v[96:97], 0, s[100:101]
	global_load_lds_dwordx4 v[98:99], off
	s_add_i32 m0, s98, 0x400
	v_lshl_add_u64 v[98:99], v[98:99], 0, s[100:101]
	global_load_lds_dwordx4 v[100:101], off
	s_add_i32 m0, s98, 0x1800
	v_lshl_add_u64 v[100:101], v[100:101], 0, s[100:101]
	global_load_lds_dwordx4 v[102:103], off
	s_add_i32 m0, s98, 0x800
	v_lshl_add_u64 v[102:103], v[102:103], 0, s[100:101]
	global_load_lds_dwordx4 v[104:105], off
	s_add_i32 m0, s98, 0x1c00
	v_lshl_add_u64 v[104:105], v[104:105], 0, s[100:101]
	global_load_lds_dwordx4 v[106:107], off
	s_add_i32 m0, s98, 0xc00
	v_lshl_add_u64 v[106:107], v[106:107], 0, s[100:101]
	global_load_lds_dwordx4 v[108:109], off
	v_lshl_add_u64 v[108:109], v[108:109], 0, s[100:101]
.Lmx1_skip:
	s_add_i32 s46, s46, -1
	s_xor_b32 s98, s98, 0x2000
	s_xor_b32 s99, s99, 0x2000
	s_nop 11
	v_cvt_pknorm_u16_f32 v36, v36, v37
	v_cvt_pknorm_u16_f32 v37, v38, v39
	v_cvt_pknorm_u16_f32 v38, v40, v41
	v_cvt_pknorm_u16_f32 v39, v42, v43
	v_cvt_pknorm_u16_f32 v40, v44, v45
	v_cvt_pknorm_u16_f32 v41, v46, v47
	v_mfma_f32_32x32x16_bf16 v[20:35], v[172:175], v[36:39], v[20:35]
	v_cvt_pknorm_u16_f32 v42, v48, v49
	v_cvt_pknorm_u16_f32 v43, v50, v51
	v_or3_b32 v48, v127, v43, v42
	v_add_u32_e32 v69, 0x80, v69
	s_andn2_b64 vcc, exec, s[36:37]
	v_mfma_f32_32x32x16_bf16 v[4:19], v[176:179], v[36:39], v[4:19]
	v_mfma_f32_32x32x16_bf16 v[20:35], v[180:183], v[40:43], v[20:35]
	v_mfma_f32_16x16x32_bf16 v[44:47], v[70:73], v[36:39], v[90:93]
	v_or3_b32 v39, v48, v40, v39
	v_or3_b32 v37, v39, v41, v37
	v_or3_b32 v127, v37, v36, v38
	v_mfma_f32_32x32x16_bf16 v[4:19], v[184:187], v[40:43], v[4:19]
	v_mfma_f32_16x16x32_bf16 v[90:93], v[70:73], v[40:43], v[44:47]
	s_cbranch_vccz .LBB0_365
.LBB0_362:
	s_add_i32 s46, s46, 1
	s_cmp_ge_i32 s46, s16
	s_cselect_b64 s[36:37], -1, 0
	s_waitcnt vmcnt(8)
	s_cbranch_scc0 .LBB0_361
	s_waitcnt vmcnt(0)
	s_branch .LBB0_361

; #define LAS __attribute__((address_space(3)))
; #define BA_LOAD(kn, vn, kt_) do { const int kb_ = kb_first + 32 * (kt_); \
;         _Pragma("unroll") for (int ii = 0; ii < 4; ++ii) { const size_t row_ = (size_t)(res + dil * (kb_ + vr + 8 * ii)); \
;             kn[ii] = *(const v4u*)(Kb + row_ * kpitch + 8 * vc); vn[ii] = *(const v4u*)(Vb + row_ * vpitch + 8 * vc); } } while (0)
; #define BA_LOAD(kn, vn, kt_) do { const int kb_ = kb_first + 32 * (kt_); \
;         _Pragma("unroll") for (int ii = 0; ii < 4; ++ii) { const size_t row_ = (size_t)(res + dil * (kb_ + vr + 8 * ii)); \
;             kn[ii] = *(const v4u*)(Kb + row_ * kpitch + 8 * vc); vn[ii] = *(const v4u*)(Vb + row_ * vpitch + 8 * vc); } } while (0)
; __device__ __forceinline__ void band_branch_fast(f32x16& o0, f32x16& o1, f32x4& lsum, unsigned& orw, const bf16x8 (&qf)[4], ...
;     ...
;     int kt_lo = 0, kt_hi = ntiles;
;     if (kb_first < 0) kt_lo = (-kb_first) >> 5;
;     { const int mx = (L - kb_first) >> 5; if (mx < kt_hi) kt_hi = mx; }
;     const int i5 = lane & 31, hh = lane >> 5;
;     const int pi = (i5 & 0x13) | (((i5 >> 2) & 1) << 3) | (((i5 >> 3) & 1) << 2);
;     const int vr = lane >> 3, vc = lane & 7;
;     LAS unsigned char* kst = vst + 4096;
;     const LAS unsigned char* trb = vst + (8 * hh + ((lane & 15) >> 2)) * 128 + (16 * ((lane >> 4) & 1) + 4 * (lane & 3)) * 2;
;     const LAS unsigned char* krd = kst + pi * 128;
;     v4u kn[4], vn[4];
;     ...
;     if (kt_lo < kt_hi) BA_LOAD(kn, vn, kt_lo);
; __device__ __forceinline__ void mixer_a_phase(const bf16* AQ, const bf16* AK, const bf16* AV  , bf16* O, float* ST, float* ML, const float* rel_bias, LAS unsigned char* lds, int G, int blk, int tid, int lane, int wave) {
;     ...
;                 f32x4 lsum = {0.f, 0.f, 0.f, 0.f}; unsigned orw = 0u;
;                 band_branch_fast(o0, o1, lsum, orw, qf, Kb, 512, Vb, 512, 16, r, 512, 32 * (a - 2), 5, tab + 2 * TA_LEN, -(32 * a + i5) + 64 + TA_OFF + 8 * hh, vst, lane);
.LBB0_390:
	s_andn2_b64 vcc, exec, s[10:11]
	s_cbranch_vccnz .LBB0_395
	v_and_b32_e32 v58, 7, v1
	v_xor_b32_e32 v59, v58, v196
	v_sub_u32_e32 v58, v59, v58
	v_lshlrev_b32_e32 v64, 4, v58
	v_ashrrev_i32_e32 v65, 31, v64
	v_lshl_add_u64 v[66:67], v[152:153], 0, v[64:65]
	v_readlane_b32 s98, v254, 59
	s_mov_b64 s[100:101], 0x80000
	v_add_u32_e32 v58, s25, v219
	v_ashrrev_i32_e32 v59, 31, v58
	v_lshlrev_b64 v[58:59], 10, v[58:59]
	v_lshl_add_u64 v[106:107], v[66:67], 0, v[58:59]
	v_lshl_add_u64 v[108:109], v[154:155], 0, v[58:59]
	v_add_u32_e32 v58, s25, v220
	v_ashrrev_i32_e32 v59, 31, v58
	v_lshlrev_b64 v[58:59], 10, v[58:59]
	v_lshl_add_u64 v[110:111], v[66:67], 0, v[58:59]
	v_lshl_add_u64 v[112:113], v[154:155], 0, v[58:59]
	v_add_u32_e32 v58, s25, v221
	v_ashrrev_i32_e32 v59, 31, v58
	v_lshlrev_b64 v[58:59], 10, v[58:59]
	v_lshl_add_u64 v[114:115], v[66:67], 0, v[58:59]
	v_lshl_add_u64 v[116:117], v[154:155], 0, v[58:59]
	v_add_u32_e32 v58, s25, v222
	v_ashrrev_i32_e32 v59, 31, v58
	v_lshlrev_b64 v[58:59], 10, v[58:59]
	v_lshl_add_u64 v[118:119], v[66:67], 0, v[58:59]
	v_lshl_add_u64 v[120:121], v[154:155], 0, v[58:59]
	s_lshl_b32 s98, s98, 14
	s_add_i32 s98, s98, 0x4000
	s_mov_b32 s99, 0
	s_add_i32 m0, s98, 0x1000
	s_nop 0
	global_load_lds_dwordx4 v[106:107], off
	s_add_i32 m0, s98, 0x0
	v_lshl_add_u64 v[106:107], v[106:107], 0, s[100:101]
	global_load_lds_dwordx4 v[108:109], off
	s_add_i32 m0, s98, 0x1400
	v_lshl_add_u64 v[108:109], v[108:109], 0, s[100:101]
	global_load_lds_dwordx4 v[110:111], off
	s_add_i32 m0, s98, 0x400
	v_lshl_add_u64 v[110:111], v[110:111], 0, s[100:101]
	global_load_lds_dwordx4 v[112:113], off
	s_add_i32 m0, s98, 0x1800
	v_lshl_add_u64 v[112:113], v[112:113], 0, s[100:101]
	global_load_lds_dwordx4 v[114:115], off
	s_add_i32 m0, s98, 0x800
	v_lshl_add_u64 v[114:115], v[114:115], 0, s[100:101]
	global_load_lds_dwordx4 v[116:117], off
	s_add_i32 m0, s98, 0x1c00
	v_lshl_add_u64 v[116:117], v[116:117], 0, s[100:101]
	global_load_lds_dwordx4 v[118:119], off
	s_add_i32 m0, s98, 0xc00
	v_lshl_add_u64 v[118:119], v[118:119], 0, s[100:101]
	global_load_lds_dwordx4 v[120:121], off
	v_lshl_add_u64 v[120:121], v[120:121], 0, s[100:101]
	s_add_i32 s0, s34, 1
	s_cmp_lt_u32 s0, s35
	s_cbranch_scc0 .Lmx2_p1
	s_add_i32 m0, s98, 0x3000
	s_nop 0
	global_load_lds_dwordx4 v[106:107], off
	s_add_i32 m0, s98, 0x2000
	v_lshl_add_u64 v[106:107], v[106:107], 0, s[100:101]
	global_load_lds_dwordx4 v[108:109], off
	s_add_i32 m0, s98, 0x3400
	v_lshl_add_u64 v[108:109], v[108:109], 0, s[100:101]
	global_load_lds_dwordx4 v[110:111], off
	s_add_i32 m0, s98, 0x2400
	v_lshl_add_u64 v[110:111], v[110:111], 0, s[100:101]
	global_load_lds_dwordx4 v[112:113], off
	s_add_i32 m0, s98, 0x3800
	v_lshl_add_u64 v[112:113], v[112:113], 0, s[100:101]
	global_load_lds_dwordx4 v[114:115], off
	s_add_i32 m0, s98, 0x2800
	v_lshl_add_u64 v[114:115], v[114:115], 0, s[100:101]
	global_load_lds_dwordx4 v[116:117], off
	s_add_i32 m0, s98, 0x3c00
	v_lshl_add_u64 v[116:117], v[116:117], 0, s[100:101]
	global_load_lds_dwordx4 v[118:119], off
	s_add_i32 m0, s98, 0x2c00
	v_lshl_add_u64 v[118:119], v[118:119], 0, s[100:101]
	global_load_lds_dwordx4 v[120:121], off
	v_lshl_add_u64 v[120:121], v[120:121], 0, s[100:101]
.Lmx2_p1:
	v_mov_b32_e32 v54, 0
	v_mov_b32_e32 v136, 0
	v_mov_b32_e32 v4, v224
	v_mov_b32_e32 v2, v223
	s_mov_b32 s0, s34
	v_mov_b32_e32 v55, v54
	v_mov_b32_e32 v56, v54
	v_mov_b32_e32 v57, v54
	s_branch .LBB0_393
; #define LAS __attribute__((address_space(3)))
; #define BA_TR(off_) __builtin_bit_cast(s16x4, __builtin_amdgcn_ds_read_tr16_b64_v4i16((LAS v4i16_t*)(trb + (off_))))
; #define BA_TR(off_) __builtin_bit_cast(s16x4, __builtin_amdgcn_ds_read_tr16_b64_v4i16((LAS v4i16_t*)(trb + (off_))))
; __device__ __forceinline__ void band_branch_fast(f32x16& o0, f32x16& o1, f32x4& lsum, unsigned& orw, const bf16x8 (&qf)[4], ...
;     ...
;     for (int kt = kt_lo; kt < kt_hi; ++kt) {
; #pragma unroll
;         for (int ii = 0; ii < 4; ++ii) { const int r_ = vr + 8 * ii; *(LAS v4u*)(kst + r_ * 128 + ((vc ^ (r_ & 7)) * 16)) = kn[ii]; *(LAS v4u*)(vst + r_ * 128 + vc * 16) = vn[ii]; }
;         if (kt + 1 < kt_hi) BA_LOAD(kn, vn, kt + 1);
;         bf16x8 kf[4];
; #pragma unroll
;         for (int d0 = 0; d0 < 4; ++d0) kf[d0] = *(const LAS bf16x8*)(krd + (((2 * d0 + hh) ^ (pi & 7)) * 16));
;         const LAS float* tp = tab + (kb_first + 32 * kt + tboff);
;         f32x16 s;
; #pragma unroll
;         for (int r = 0; r < 16; ++r) s[r] = tp[(r & 7) + 16 * (r >> 3)];
;         s16x4 vt[8];
; #pragma unroll
;         for (int i = 0; i < 8; ++i) vt[i] = BA_TR((i >> 2) * 2048 + ((i >> 1) & 1) * 64 + (i & 1) * 512);
;         __builtin_amdgcn_sched_barrier(0);
; #pragma unroll
;         for (int d0 = 0; d0 < 4; ++d0) s = __builtin_amdgcn_mfma_f32_32x32x16_bf16(kf[d0], qf[d0], s, 0, 0, 0);
;         __builtin_amdgcn_sched_barrier(0);
;         v4u p0, p1;
;     ...
;         p0.x = BA_PKN(s[0], s[1]); p0.y = BA_PKN(s[2], s[3]); p0.z = BA_PKN(s[4], s[5]); p0.w = BA_PKN(s[6], s[7]);
;         p1.x = BA_PKN(s[8], s[9]); p1.y = BA_PKN(s[10], s[11]); p1.z = BA_PKN(s[12], s[13]); p1.w = BA_PKN(s[14], s[15]);
;     ...
;         orw |= (p0.x | p0.y | p0.z) | (p0.w | p1.x | p1.y) | (p1.z | p1.w);
;         const bf16x8 pk0 = __builtin_bit_cast(bf16x8, p0), pk1 = __builtin_bit_cast(bf16x8, p1);
;         lsum = __builtin_amdgcn_mfma_f32_16x16x32_bf16(onesA, pk0, lsum, 0, 0, 0); lsum = __builtin_amdgcn_mfma_f32_16x16x32_bf16(onesA, pk1, lsum, 0, 0, 0);
;         o0 = __builtin_amdgcn_mfma_f32_32x32x16_bf16(BA_VF(0), pk0, o0, 0, 0, 0); o1 = __builtin_amdgcn_mfma_f32_32x32x16_bf16(BA_VF(2), pk0, o1, 0, 0, 0);
;         o0 = __builtin_amdgcn_mfma_f32_32x32x16_bf16(BA_VF(4), pk1, o0, 0, 0, 0); o1 = __builtin_amdgcn_mfma_f32_32x32x16_bf16(BA_VF(6), pk1, o1, 0, 0, 0);
.LBB0_392:
	v_add3_u32 v5, v195, v200, s99
	v_add3_u32 v38, v195, v201, s99
	ds_read_b128 v[130:133], v5 offset:20480
	ds_read_b128 v[186:189], v38 offset:20480
	v_add3_u32 v5, v195, v202, s99
	v_add3_u32 v38, v195, v203, s99
	ds_read_b128 v[226:229], v5 offset:20480
	ds_read_b128 v[230:233], v38 offset:20480
	ds_read2_b32 v[38:39], v2 offset1:1
	ds_read2_b32 v[40:41], v2 offset0:2 offset1:3
	ds_read2_b32 v[42:43], v2 offset0:4 offset1:5
	ds_read2_b32 v[44:45], v2 offset0:6 offset1:7
	ds_read2_b32 v[46:47], v2 offset0:16 offset1:17
	ds_read2_b32 v[48:49], v2 offset0:18 offset1:19
	ds_read2_b32 v[50:51], v2 offset0:20 offset1:21
	ds_read2_b32 v[52:53], v2 offset0:22 offset1:23
	v_add3_u32 v5, v194, v193, s99
	ds_read_b64_tr_b16 v[234:235], v5 offset:16384
	ds_read_b64_tr_b16 v[236:237], v5 offset:16896
	ds_read_b64_tr_b16 v[240:241], v5 offset:16960
	ds_read_b64_tr_b16 v[238:239], v5 offset:16448
	ds_read_b64_tr_b16 v[242:243], v5 offset:18432
	ds_read_b64_tr_b16 v[244:245], v5 offset:18944
	ds_read_b64_tr_b16 v[248:249], v5 offset:19008
	ds_read_b64_tr_b16 v[246:247], v5 offset:18496
	s_waitcnt lgkmcnt(8)
	v_mfma_f32_32x32x16_bf16 v[38:53], v[130:133], v[74:77], v[38:53]
	v_mfma_f32_32x32x16_bf16 v[38:53], v[186:189], v[78:81], v[38:53]
	v_mfma_f32_32x32x16_bf16 v[38:53], v[226:229], v[82:85], v[38:53]
	v_mfma_f32_32x32x16_bf16 v[38:53], v[230:233], v[86:89], v[38:53]
	s_waitcnt lgkmcnt(0)
	s_add_i32 s0, s0, 1
	s_cmp_lt_u32 s0, s35
	s_cbranch_scc0 .Lmx2_skip
	s_add_i32 m0, s98, 0x1000
	s_nop 0
	global_load_lds_dwordx4 v[106:107], off
	s_add_i32 m0, s98, 0x0
	v_lshl_add_u64 v[106:107], v[106:107], 0, s[100:101]
	global_load_lds_dwordx4 v[108:109], off
	s_add_i32 m0, s98, 0x1400
	v_lshl_add_u64 v[108:109], v[108:109], 0, s[100:101]
	global_load_lds_dwordx4 v[110:111], off
	s_add_i32 m0, s98, 0x400
	v_lshl_add_u64 v[110:111], v[110:111], 0, s[100:101]
	global_load_lds_dwordx4 v[112:113], off
	s_add_i32 m0, s98, 0x1800
	v_lshl_add_u64 v[112:113], v[112:113], 0, s[100:101]
	global_load_lds_dwordx4 v[114:115], off
	s_add_i32 m0, s98, 0x800
	v_lshl_add_u64 v[114:115], v[114:115], 0, s[100:101]
	global_load_lds_dwordx4 v[116:117], off
	s_add_i32 m0, s98, 0x1c00
	v_lshl_add_u64 v[116:117], v[116:117], 0, s[100:101]
	global_load_lds_dwordx4 v[118:119], off
	s_add_i32 m0, s98, 0xc00
	v_lshl_add_u64 v[118:119], v[118:119], 0, s[100:101]
	global_load_lds_dwordx4 v[120:121], off
	v_lshl_add_u64 v[120:121], v[120:121], 0, s[100:101]
.Lmx2_skip:
	s_add_i32 s0, s0, -1
	s_xor_b32 s98, s98, 0x2000
	s_xor_b32 s99, s99, 0x2000
	s_nop 11
	v_cvt_pknorm_u16_f32 v38, v38, v39
	v_cvt_pknorm_u16_f32 v39, v40, v41
	v_cvt_pknorm_u16_f32 v40, v42, v43
	v_cvt_pknorm_u16_f32 v41, v44, v45
	v_cvt_pknorm_u16_f32 v42, v46, v47
	v_cvt_pknorm_u16_f32 v43, v48, v49
	v_mfma_f32_32x32x16_bf16 v[22:37], v[234:237], v[38:41], v[22:37]
	v_cvt_pknorm_u16_f32 v44, v50, v51
	v_cvt_pknorm_u16_f32 v45, v52, v53
	v_or3_b32 v5, v136, v45, v44
	v_or3_b32 v5, v5, v42, v41
	v_or3_b32 v5, v5, v43, v39
	v_or3_b32 v136, v5, v38, v40
	v_add_u32_e32 v2, 0x80, v2
	v_mfma_f32_32x32x16_bf16 v[6:21], v[238:241], v[38:41], v[6:21]
	s_andn2_b64 vcc, exec, s[10:11]
	v_mfma_f32_32x32x16_bf16 v[22:37], v[242:245], v[42:45], v[22:37]
	v_mfma_f32_16x16x32_bf16 v[46:49], v[70:73], v[38:41], v[54:57]
	v_mfma_f32_32x32x16_bf16 v[6:21], v[246:249], v[42:45], v[6:21]
	v_mfma_f32_16x16x32_bf16 v[54:57], v[70:73], v[42:45], v[46:49]
	s_cbranch_vccz .LBB0_396
.LBB0_393:
	s_add_i32 s0, s0, 1
	s_cmp_ge_u32 s0, s35
	s_cselect_b64 s[10:11], -1, 0
	s_waitcnt vmcnt(8)
	s_cbranch_scc0 .LBB0_392
	s_waitcnt vmcnt(0)
	s_branch .LBB0_392

; #define LAS __attribute__((address_space(3)))
; #define BA_TR(off_) __builtin_bit_cast(s16x4, __builtin_amdgcn_ds_read_tr16_b64_v4i16((LAS v4i16_t*)(trb + (off_))))
; #define BA_TR(off_) __builtin_bit_cast(s16x4, __builtin_amdgcn_ds_read_tr16_b64_v4i16((LAS v4i16_t*)(trb + (off_))))
; __device__ __forceinline__ void band_branch_fast(f32x16& o0, f32x16& o1, f32x4& lsum, unsigned& orw, const bf16x8 (&qf)[4], ...
;     ...
;     if (kt_lo < kt_hi) BA_LOAD(kn, vn, kt_lo);
;     for (int kt = kt_lo; kt < kt_hi; ++kt) {
; #pragma unroll
;         for (int ii = 0; ii < 4; ++ii) { const int r_ = vr + 8 * ii; *(LAS v4u*)(kst + r_ * 128 + ((vc ^ (r_ & 7)) * 16)) = kn[ii]; *(LAS v4u*)(vst + r_ * 128 + vc * 16) = vn[ii]; }
;         if (kt + 1 < kt_hi) BA_LOAD(kn, vn, kt + 1);
;         bf16x8 kf[4];
; #pragma unroll
;         for (int d0 = 0; d0 < 4; ++d0) kf[d0] = *(const LAS bf16x8*)(krd + (((2 * d0 + hh) ^ (pi & 7)) * 16));
;         const LAS float* tp = tab + (kb_first + 32 * kt + tboff);
;         f32x16 s;
; #pragma unroll
;         for (int r = 0; r < 16; ++r) s[r] = tp[(r & 7) + 16 * (r >> 3)];
;         s16x4 vt[8];
; #pragma unroll
;         for (int i = 0; i < 8; ++i) vt[i] = BA_TR((i >> 2) * 2048 + ((i >> 1) & 1) * 64 + (i & 1) * 512);
;         __builtin_amdgcn_sched_barrier(0);
; #pragma unroll
;         for (int d0 = 0; d0 < 4; ++d0) s = __builtin_amdgcn_mfma_f32_32x32x16_bf16(kf[d0], qf[d0], s, 0, 0, 0);
;         __builtin_amdgcn_sched_barrier(0);
;         v4u p0, p1;
;     ...
;         p0.x = BA_PKN(s[0], s[1]); p0.y = BA_PKN(s[2], s[3]); p0.z = BA_PKN(s[4], s[5]); p0.w = BA_PKN(s[6], s[7]);
;         p1.x = BA_PKN(s[8], s[9]); p1.y = BA_PKN(s[10], s[11]); p1.z = BA_PKN(s[12], s[13]); p1.w = BA_PKN(s[14], s[15]);
;     ...
;         orw |= (p0.x | p0.y | p0.z) | (p0.w | p1.x | p1.y) | (p1.z | p1.w);
;         const bf16x8 pk0 = __builtin_bit_cast(bf16x8, p0), pk1 = __builtin_bit_cast(bf16x8, p1);
;         lsum = __builtin_amdgcn_mfma_f32_16x16x32_bf16(onesA, pk0, lsum, 0, 0, 0); lsum = __builtin_amdgcn_mfma_f32_16x16x32_bf16(onesA, pk1, lsum, 0, 0, 0);
;         o0 = __builtin_amdgcn_mfma_f32_32x32x16_bf16(BA_VF(0), pk0, o0, 0, 0, 0); o1 = __builtin_amdgcn_mfma_f32_32x32x16_bf16(BA_VF(2), pk0, o1, 0, 0, 0);
;         o0 = __builtin_amdgcn_mfma_f32_32x32x16_bf16(BA_VF(4), pk1, o0, 0, 0, 0); o1 = __builtin_amdgcn_mfma_f32_32x32x16_bf16(BA_VF(6), pk1, o1, 0, 0, 0);
.LBB0_396:
	v_and_b32_e32 v58, 7, v1
	v_xor_b32_e32 v59, v58, v196
	v_sub_u32_e32 v58, v59, v58
	v_lshlrev_b32_e32 v64, 4, v58
	v_ashrrev_i32_e32 v65, 31, v64
	v_readlane_b32 s98, v254, 59
	v_lshl_add_u64 v[106:107], v[158:159], 0, v[64:65]
	v_mov_b64_e32 v[108:109], v[160:161]
	v_lshl_add_u64 v[110:111], v[162:163], 0, v[64:65]
	v_mov_b64_e32 v[112:113], v[164:165]
	v_lshl_add_u64 v[114:115], v[166:167], 0, v[64:65]
	v_mov_b64_e32 v[116:117], v[168:169]
	v_lshl_add_u64 v[118:119], v[170:171], 0, v[64:65]
	v_mov_b64_e32 v[120:121], v[172:173]
	s_lshl_b32 s98, s98, 14
	s_add_i32 s98, s98, 0x4000
	s_mov_b32 s99, 0
	s_add_i32 m0, s98, 0x1000
	s_nop 0
	global_load_lds_dwordx4 v[106:107], off
	s_add_i32 m0, s98, 0x0
	v_lshl_add_u64 v[106:107], v[106:107], 0, s[20:21]
	global_load_lds_dwordx4 v[108:109], off
	s_add_i32 m0, s98, 0x1400
	v_lshl_add_u64 v[108:109], v[108:109], 0, s[20:21]
	global_load_lds_dwordx4 v[110:111], off
	s_add_i32 m0, s98, 0x400
	v_lshl_add_u64 v[110:111], v[110:111], 0, s[20:21]
	global_load_lds_dwordx4 v[112:113], off
	s_add_i32 m0, s98, 0x1800
	v_lshl_add_u64 v[112:113], v[112:113], 0, s[20:21]
	global_load_lds_dwordx4 v[114:115], off
	s_add_i32 m0, s98, 0x800
	v_lshl_add_u64 v[114:115], v[114:115], 0, s[20:21]
	global_load_lds_dwordx4 v[116:117], off
	s_add_i32 m0, s98, 0x1c00
	v_lshl_add_u64 v[116:117], v[116:117], 0, s[20:21]
	global_load_lds_dwordx4 v[118:119], off
	s_add_i32 m0, s98, 0xc00
	v_lshl_add_u64 v[118:119], v[118:119], 0, s[20:21]
	global_load_lds_dwordx4 v[120:121], off
	v_lshl_add_u64 v[120:121], v[120:121], 0, s[20:21]
	s_add_i32 s0, s36, 1
	s_cmp_lt_u32 s0, s37
	s_cbranch_scc0 .Lmx3_p1
	s_add_i32 m0, s98, 0x3000
	s_nop 0
	global_load_lds_dwordx4 v[106:107], off
	s_add_i32 m0, s98, 0x2000
	v_lshl_add_u64 v[106:107], v[106:107], 0, s[20:21]
	global_load_lds_dwordx4 v[108:109], off
	s_add_i32 m0, s98, 0x3400
	v_lshl_add_u64 v[108:109], v[108:109], 0, s[20:21]
	global_load_lds_dwordx4 v[110:111], off
	s_add_i32 m0, s98, 0x2400
	v_lshl_add_u64 v[110:111], v[110:111], 0, s[20:21]
	global_load_lds_dwordx4 v[112:113], off
	s_add_i32 m0, s98, 0x3800
	v_lshl_add_u64 v[112:113], v[112:113], 0, s[20:21]
	global_load_lds_dwordx4 v[114:115], off
	s_add_i32 m0, s98, 0x2800
	v_lshl_add_u64 v[114:115], v[114:115], 0, s[20:21]
	global_load_lds_dwordx4 v[116:117], off
	s_add_i32 m0, s98, 0x3c00
	v_lshl_add_u64 v[116:117], v[116:117], 0, s[20:21]
	global_load_lds_dwordx4 v[118:119], off
	s_add_i32 m0, s98, 0x2c00
	v_lshl_add_u64 v[118:119], v[118:119], 0, s[20:21]
	global_load_lds_dwordx4 v[120:121], off
	v_lshl_add_u64 v[120:121], v[120:121], 0, s[20:21]
.Lmx3_p1:
	v_mov_b32_e32 v2, v225
	s_mov_b32 s0, s36
	s_branch .LBB0_398
.LBB0_397:
	v_add3_u32 v38, v195, v200, s99
	v_add3_u32 v39, v195, v201, s99
	ds_read_b128 v[186:189], v38 offset:20480
	ds_read_b128 v[226:229], v39 offset:20480
	v_add3_u32 v38, v195, v202, s99
	v_add3_u32 v39, v195, v203, s99
	ds_read_b128 v[230:233], v38 offset:20480
	ds_read_b128 v[234:237], v39 offset:20480
	ds_read2_b32 v[38:39], v2 offset1:1
	ds_read2_b32 v[40:41], v2 offset0:2 offset1:3
	ds_read2_b32 v[42:43], v2 offset0:4 offset1:5
	ds_read2_b32 v[44:45], v2 offset0:6 offset1:7
	ds_read2_b32 v[46:47], v2 offset0:16 offset1:17
	ds_read2_b32 v[48:49], v2 offset0:18 offset1:19
	ds_read2_b32 v[50:51], v2 offset0:20 offset1:21
	ds_read2_b32 v[52:53], v2 offset0:22 offset1:23
	v_add3_u32 v137, v194, v193, s99
	ds_read_b64_tr_b16 v[238:239], v137 offset:16384
	ds_read_b64_tr_b16 v[240:241], v137 offset:16896
	ds_read_b64_tr_b16 v[244:245], v137 offset:16960
	ds_read_b64_tr_b16 v[242:243], v137 offset:16448
	ds_read_b64_tr_b16 v[246:247], v137 offset:18432
	ds_read_b64_tr_b16 v[248:249], v137 offset:18944
	ds_read_b64_tr_b16 v[252:253], v137 offset:19008
	ds_read_b64_tr_b16 v[250:251], v137 offset:18496
	s_waitcnt lgkmcnt(8)
	v_mfma_f32_32x32x16_bf16 v[38:53], v[186:189], v[74:77], v[38:53]
	v_mfma_f32_32x32x16_bf16 v[38:53], v[226:229], v[78:81], v[38:53]
	v_mfma_f32_32x32x16_bf16 v[38:53], v[230:233], v[82:85], v[38:53]
	v_mfma_f32_32x32x16_bf16 v[38:53], v[234:237], v[86:89], v[38:53]
	s_waitcnt lgkmcnt(0)
	s_add_i32 s0, s0, 1
	s_cmp_lt_u32 s0, s37
	s_cbranch_scc0 .Lmx3_skip
	s_add_i32 m0, s98, 0x1000
	s_nop 0
	global_load_lds_dwordx4 v[106:107], off
	s_add_i32 m0, s98, 0x0
	v_lshl_add_u64 v[106:107], v[106:107], 0, s[20:21]
	global_load_lds_dwordx4 v[108:109], off
	s_add_i32 m0, s98, 0x1400
	v_lshl_add_u64 v[108:109], v[108:109], 0, s[20:21]
	global_load_lds_dwordx4 v[110:111], off
	s_add_i32 m0, s98, 0x400
	v_lshl_add_u64 v[110:111], v[110:111], 0, s[20:21]
	global_load_lds_dwordx4 v[112:113], off
	s_add_i32 m0, s98, 0x1800
	v_lshl_add_u64 v[112:113], v[112:113], 0, s[20:21]
	global_load_lds_dwordx4 v[114:115], off
	s_add_i32 m0, s98, 0x800
	v_lshl_add_u64 v[114:115], v[114:115], 0, s[20:21]
	global_load_lds_dwordx4 v[116:117], off
	s_add_i32 m0, s98, 0x1c00
	v_lshl_add_u64 v[116:117], v[116:117], 0, s[20:21]
	global_load_lds_dwordx4 v[118:119], off
	s_add_i32 m0, s98, 0xc00
	v_lshl_add_u64 v[118:119], v[118:119], 0, s[20:21]
	global_load_lds_dwordx4 v[120:121], off
	v_lshl_add_u64 v[120:121], v[120:121], 0, s[20:21]
.Lmx3_skip:
	s_add_i32 s0, s0, -1
	s_xor_b32 s98, s98, 0x2000
	s_xor_b32 s99, s99, 0x2000
	s_nop 11
	v_cvt_pknorm_u16_f32 v38, v38, v39
	v_cvt_pknorm_u16_f32 v39, v40, v41
	v_cvt_pknorm_u16_f32 v40, v42, v43
	v_cvt_pknorm_u16_f32 v41, v44, v45
	v_cvt_pknorm_u16_f32 v42, v46, v47
	v_cvt_pknorm_u16_f32 v43, v48, v49
	v_mfma_f32_32x32x16_bf16 v[22:37], v[238:241], v[38:41], v[22:37]
	v_cvt_pknorm_u16_f32 v44, v50, v51
	v_cvt_pknorm_u16_f32 v45, v52, v53
	v_or3_b32 v50, v136, v45, v44
	v_add_u32_e32 v2, 0x80, v2
	v_mfma_f32_32x32x16_bf16 v[6:21], v[242:245], v[38:41], v[6:21]
	s_andn2_b64 vcc, exec, s[10:11]
	v_mfma_f32_16x16x32_bf16 v[46:49], v[70:73], v[38:41], v[54:57]
	v_or3_b32 v41, v50, v42, v41
	v_or3_b32 v39, v41, v43, v39
	v_or3_b32 v136, v39, v38, v40
	v_mfma_f32_32x32x16_bf16 v[22:37], v[246:249], v[42:45], v[22:37]
	v_mfma_f32_32x32x16_bf16 v[6:21], v[250:253], v[42:45], v[6:21]
	v_mfma_f32_16x16x32_bf16 v[54:57], v[70:73], v[42:45], v[46:49]
	s_cbranch_vccz .LBB0_400
.LBB0_398:
	s_add_i32 s0, s0, 1
	s_cmp_ge_u32 s0, s37
	s_cselect_b64 s[10:11], -1, 0
	s_waitcnt vmcnt(8)
	s_cbranch_scc0 .LBB0_397
	s_waitcnt vmcnt(0)
	s_branch .LBB0_397
